# instruction selection: gather address calc 4 to 2 VALU per edge (shift + v_and_or) in both main loops
# baseline (speedup 1.0000x reference)
.Lcensus_skip:
	s_and_saveexec_b64 s[10:11], s[8:9]
	s_cbranch_execz .LBB2_285
	v_lshlrev_b32_e32 v109, 5, v44
	global_load_dwordx4 v[100:103], v109, s[60:61]
	global_load_dwordx4 v[104:107], v109, s[60:61] offset:16
	v_ashrrev_i32_e32 v65, 31, v64
	v_lshl_add_u64 v[110:111], v[64:65], 2, s[58:59]
	global_load_dword v108, v[110:111], off
	s_and_b64 vcc, exec, s[4:5]
	s_cbranch_vccz .LBB2_282
	v_add_u32_e32 v2, 8, v46
	v_mov_b32_e32 v55, 0x3f80
	v_mov_b32_e32 v54, 1.0
	v_cmp_le_u32_e32 vcc, v2, v47
	v_mov_b32_e32 v5, 0
	v_mov_b32_e32 v4, 0
	v_mov_b32_e32 v3, 0
	v_mov_b32_e32 v2, 0
	v_mov_b32_e32 v9, 0
	v_mov_b32_e32 v8, 0
	v_mov_b32_e32 v7, 0
	v_mov_b32_e32 v6, 0
	v_mov_b32_e32 v57, v46
	s_and_saveexec_b64 s[2:3], vcc
	s_cbranch_execz .LBB2_273
	v_mov_b32_e32 v5, 0
	v_lshlrev_b32_e32 v43, 4, v44
	s_mov_b32 s86, 0x3fffe0
	v_lshlrev_b32_e32 v56, 2, v46
	s_mov_b64 s[12:13], 0
	v_mov_b32_e32 v57, v46
	v_mov_b32_e32 v4, v5
	v_mov_b32_e32 v3, v5
	v_mov_b32_e32 v2, v5
	v_mov_b32_e32 v9, v5
	v_mov_b32_e32 v8, v5
	v_mov_b32_e32 v7, v5
	v_mov_b32_e32 v6, v5
.LBB2_271:
	ds_read2_b32 v[10:11], v56 offset1:1
	ds_read2_b32 v[12:13], v56 offset0:2 offset1:3
	ds_read2_b32 v[14:15], v56 offset0:4 offset1:5
	ds_read2_b32 v[16:17], v56 offset0:6 offset1:7
	v_add_u32_e32 v56, 32, v56
	s_waitcnt lgkmcnt(3)
	v_lshlrev_b32_e32 v58, 5, v10
	v_and_or_b32 v58, v58, s86, v43
	v_lshlrev_b32_e32 v59, 5, v11
	v_and_or_b32 v59, v59, s86, v43
	s_waitcnt lgkmcnt(2)
	v_lshlrev_b32_e32 v60, 5, v12
	v_and_or_b32 v60, v60, s86, v43
	v_lshlrev_b32_e32 v61, 5, v13
	v_and_or_b32 v61, v61, s86, v43
	s_waitcnt lgkmcnt(1)
	v_lshlrev_b32_e32 v14, 5, v14
	v_and_or_b32 v14, v14, s86, v43
	v_lshlrev_b32_e32 v15, 5, v15
	v_and_or_b32 v15, v15, s86, v43
	s_waitcnt lgkmcnt(0)
	v_lshlrev_b32_e32 v16, 5, v16
	v_and_or_b32 v16, v16, s86, v43
	v_lshlrev_b32_e32 v17, 5, v17
	v_and_or_b32 v17, v17, s86, v43
	global_load_dwordx4 v[38:41], v58, s[56:57]
	global_load_dwordx4 v[34:37], v59, s[56:57]
	global_load_dwordx4 v[30:33], v60, s[56:57]
	global_load_dwordx4 v[26:29], v61, s[56:57]
	global_load_dwordx4 v[22:25], v14, s[56:57]
	global_load_dwordx4 v[18:21], v15, s[56:57]
	global_load_dwordx4 v[10:13], v16, s[56:57]
	s_nop 0
	global_load_dwordx4 v[14:17], v17, s[56:57]
	v_mov_b32_e32 v58, v57
	v_add_u32_e32 v57, 8, v58
	v_add_u32_e32 v58, 16, v58
	v_cmp_gt_u32_e32 vcc, v58, v47
	s_or_b64 s[12:13], vcc, s[12:13]
	s_waitcnt vmcnt(7)
	v_dot2c_f32_bf16_e32 v6, v38, v55
	v_dot2c_f32_bf16_e32 v7, v38, v54
	v_dot2c_f32_bf16_e32 v8, v39, v55
	v_dot2c_f32_bf16_e32 v9, v39, v54
	v_dot2c_f32_bf16_e32 v2, v40, v55
	v_dot2c_f32_bf16_e32 v3, v40, v54
	v_dot2c_f32_bf16_e32 v4, v41, v55
	v_dot2c_f32_bf16_e32 v5, v41, v54
	s_waitcnt vmcnt(6)
	v_dot2c_f32_bf16_e32 v6, v34, v55
	v_dot2c_f32_bf16_e32 v7, v34, v54
	v_dot2c_f32_bf16_e32 v8, v35, v55
	v_dot2c_f32_bf16_e32 v9, v35, v54
	v_dot2c_f32_bf16_e32 v2, v36, v55
	v_dot2c_f32_bf16_e32 v3, v36, v54
	v_dot2c_f32_bf16_e32 v4, v37, v55
	v_dot2c_f32_bf16_e32 v5, v37, v54
	s_waitcnt vmcnt(5)
	v_dot2c_f32_bf16_e32 v6, v30, v55
	v_dot2c_f32_bf16_e32 v7, v30, v54
	v_dot2c_f32_bf16_e32 v8, v31, v55
	v_dot2c_f32_bf16_e32 v9, v31, v54
	v_dot2c_f32_bf16_e32 v2, v32, v55
	v_dot2c_f32_bf16_e32 v3, v32, v54
	v_dot2c_f32_bf16_e32 v4, v33, v55
	v_dot2c_f32_bf16_e32 v5, v33, v54
	s_waitcnt vmcnt(4)
	v_dot2c_f32_bf16_e32 v6, v26, v55
	v_dot2c_f32_bf16_e32 v7, v26, v54
	v_dot2c_f32_bf16_e32 v8, v27, v55
	v_dot2c_f32_bf16_e32 v9, v27, v54
	v_dot2c_f32_bf16_e32 v2, v28, v55
	v_dot2c_f32_bf16_e32 v3, v28, v54
	v_dot2c_f32_bf16_e32 v4, v29, v55
	v_dot2c_f32_bf16_e32 v5, v29, v54
	s_waitcnt vmcnt(3)
	v_dot2c_f32_bf16_e32 v6, v22, v55
	v_dot2c_f32_bf16_e32 v7, v22, v54
	v_dot2c_f32_bf16_e32 v8, v23, v55
	v_dot2c_f32_bf16_e32 v9, v23, v54
	v_dot2c_f32_bf16_e32 v2, v24, v55
	v_dot2c_f32_bf16_e32 v3, v24, v54
	v_dot2c_f32_bf16_e32 v4, v25, v55
	v_dot2c_f32_bf16_e32 v5, v25, v54
	s_waitcnt vmcnt(2)
	v_dot2c_f32_bf16_e32 v6, v18, v55
	v_dot2c_f32_bf16_e32 v7, v18, v54
	v_dot2c_f32_bf16_e32 v8, v19, v55
	v_dot2c_f32_bf16_e32 v9, v19, v54
	v_dot2c_f32_bf16_e32 v2, v20, v55
	v_dot2c_f32_bf16_e32 v3, v20, v54
	v_dot2c_f32_bf16_e32 v4, v21, v55
	v_dot2c_f32_bf16_e32 v5, v21, v54
	s_waitcnt vmcnt(1)
	v_dot2c_f32_bf16_e32 v6, v10, v55
	v_dot2c_f32_bf16_e32 v7, v10, v54
	v_dot2c_f32_bf16_e32 v8, v11, v55
	v_dot2c_f32_bf16_e32 v9, v11, v54
	v_dot2c_f32_bf16_e32 v2, v12, v55
	v_dot2c_f32_bf16_e32 v3, v12, v54
	v_dot2c_f32_bf16_e32 v4, v13, v55
	v_dot2c_f32_bf16_e32 v5, v13, v54
	s_waitcnt vmcnt(0)
	v_dot2c_f32_bf16_e32 v6, v14, v55
	v_dot2c_f32_bf16_e32 v7, v14, v54
	v_dot2c_f32_bf16_e32 v8, v15, v55
	v_dot2c_f32_bf16_e32 v9, v15, v54
	v_dot2c_f32_bf16_e32 v2, v16, v55
	v_dot2c_f32_bf16_e32 v3, v16, v54
	v_dot2c_f32_bf16_e32 v4, v17, v55
	v_dot2c_f32_bf16_e32 v5, v17, v54
	s_andn2_b64 exec, exec, s[12:13]
	s_cbranch_execnz .LBB2_271
	s_or_b64 exec, exec, s[12:13]

.LBB2_350:
	v_readfirstlane_b32 s91, v0
	v_and_b32_e32 v1, 0x3c0, v0
	s_lshr_b32 s91, s91, 6
	s_movk_i32 s0, 0x31f
	v_cmp_gt_u32_e32 vcc, s0, v1
	s_and_saveexec_b64 s[0:1], vcc
	s_cbranch_execz .LBB2_371
	s_andn2_b64 vcc, exec, s[4:5]
	s_cbranch_vccnz .LBB2_365
	v_add_u32_e32 v1, 8, v46
	v_mov_b32_e32 v43, 0x3f80
	v_mov_b32_e32 v42, 1.0
	v_cmp_le_u32_e32 vcc, v1, v47
	v_mov_b32_e32 v7, 0
	v_mov_b32_e32 v6, 0
	v_mov_b32_e32 v9, 0
	v_mov_b32_e32 v8, 0
	v_mov_b32_e32 v3, 0
	v_mov_b32_e32 v2, 0
	v_mov_b32_e32 v5, 0
	v_mov_b32_e32 v4, 0
	s_and_saveexec_b64 s[0:1], vcc
	s_cbranch_execz .LBB2_356
	v_lshlrev_b32_e32 v1, 4, v44
	s_mov_b32 s86, 0x3fffe0
	v_lshlrev_b32_e32 v45, 2, v46
	v_mov_b32_e32 v5, 0
	s_mov_b64 s[2:3], 0
	v_mov_b32_e32 v4, 0
	v_mov_b32_e32 v3, 0
	v_mov_b32_e32 v2, 0
	v_mov_b32_e32 v9, 0
	v_mov_b32_e32 v8, 0
	v_mov_b32_e32 v7, 0
	v_mov_b32_e32 v6, 0
.LBB2_354:
	ds_read2_b32 v[10:11], v45 offset1:1
	ds_read2_b32 v[12:13], v45 offset0:2 offset1:3
	ds_read2_b32 v[14:15], v45 offset0:4 offset1:5
	ds_read2_b32 v[16:17], v45 offset0:6 offset1:7
	v_add_u32_e32 v45, 32, v45
	s_waitcnt lgkmcnt(3)
	v_lshlrev_b32_e32 v48, 5, v10
	v_and_or_b32 v48, v48, s86, v1
	v_lshlrev_b32_e32 v49, 5, v11
	v_and_or_b32 v49, v49, s86, v1
	s_waitcnt lgkmcnt(2)
	v_lshlrev_b32_e32 v50, 5, v12
	v_and_or_b32 v50, v50, s86, v1
	v_lshlrev_b32_e32 v54, 5, v13
	v_and_or_b32 v54, v54, s86, v1
	s_waitcnt lgkmcnt(1)
	v_lshlrev_b32_e32 v55, 5, v14
	v_and_or_b32 v55, v55, s86, v1
	v_lshlrev_b32_e32 v56, 5, v15
	v_and_or_b32 v56, v56, s86, v1
	s_waitcnt lgkmcnt(0)
	v_lshlrev_b32_e32 v57, 5, v16
	v_and_or_b32 v57, v57, s86, v1
	v_lshlrev_b32_e32 v58, 5, v17
	v_and_or_b32 v58, v58, s86, v1
	global_load_dwordx4 v[38:41], v48, s[62:63]
	global_load_dwordx4 v[34:37], v49, s[62:63]
	global_load_dwordx4 v[30:33], v50, s[62:63]
	global_load_dwordx4 v[26:29], v54, s[62:63]
	global_load_dwordx4 v[22:25], v55, s[62:63]
	global_load_dwordx4 v[18:21], v56, s[62:63]
	global_load_dwordx4 v[14:17], v57, s[62:63]
	global_load_dwordx4 v[10:13], v58, s[62:63]
	v_mov_b32_e32 v48, v46
	v_add_u32_e32 v46, 8, v48
	v_add_u32_e32 v48, 16, v48
	v_cmp_gt_u32_e32 vcc, v48, v47
	s_or_b64 s[2:3], vcc, s[2:3]
	s_waitcnt vmcnt(7)
	v_dot2c_f32_bf16_e32 v6, v38, v43
	v_dot2c_f32_bf16_e32 v7, v38, v42
	v_dot2c_f32_bf16_e32 v8, v39, v43
	v_dot2c_f32_bf16_e32 v9, v39, v42
	v_dot2c_f32_bf16_e32 v2, v40, v43
	v_dot2c_f32_bf16_e32 v3, v40, v42
	v_dot2c_f32_bf16_e32 v4, v41, v43
	v_dot2c_f32_bf16_e32 v5, v41, v42
	s_waitcnt vmcnt(6)
	v_dot2c_f32_bf16_e32 v6, v34, v43
	v_dot2c_f32_bf16_e32 v7, v34, v42
	v_dot2c_f32_bf16_e32 v8, v35, v43
	v_dot2c_f32_bf16_e32 v9, v35, v42
	v_dot2c_f32_bf16_e32 v2, v36, v43
	v_dot2c_f32_bf16_e32 v3, v36, v42
	v_dot2c_f32_bf16_e32 v4, v37, v43
	v_dot2c_f32_bf16_e32 v5, v37, v42
	s_waitcnt vmcnt(5)
	v_dot2c_f32_bf16_e32 v6, v30, v43
	v_dot2c_f32_bf16_e32 v7, v30, v42
	v_dot2c_f32_bf16_e32 v8, v31, v43
	v_dot2c_f32_bf16_e32 v9, v31, v42
	v_dot2c_f32_bf16_e32 v2, v32, v43
	v_dot2c_f32_bf16_e32 v3, v32, v42
	v_dot2c_f32_bf16_e32 v4, v33, v43
	v_dot2c_f32_bf16_e32 v5, v33, v42
	s_waitcnt vmcnt(4)
	v_dot2c_f32_bf16_e32 v6, v26, v43
	v_dot2c_f32_bf16_e32 v7, v26, v42
	v_dot2c_f32_bf16_e32 v8, v27, v43
	v_dot2c_f32_bf16_e32 v9, v27, v42
	v_dot2c_f32_bf16_e32 v2, v28, v43
	v_dot2c_f32_bf16_e32 v3, v28, v42
	v_dot2c_f32_bf16_e32 v4, v29, v43
	v_dot2c_f32_bf16_e32 v5, v29, v42
	s_waitcnt vmcnt(3)
	v_dot2c_f32_bf16_e32 v6, v22, v43
	v_dot2c_f32_bf16_e32 v7, v22, v42
	v_dot2c_f32_bf16_e32 v8, v23, v43
	v_dot2c_f32_bf16_e32 v9, v23, v42
	v_dot2c_f32_bf16_e32 v2, v24, v43
	v_dot2c_f32_bf16_e32 v3, v24, v42
	v_dot2c_f32_bf16_e32 v4, v25, v43
	v_dot2c_f32_bf16_e32 v5, v25, v42
	s_waitcnt vmcnt(2)
	v_dot2c_f32_bf16_e32 v6, v18, v43
	v_dot2c_f32_bf16_e32 v7, v18, v42
	v_dot2c_f32_bf16_e32 v8, v19, v43
	v_dot2c_f32_bf16_e32 v9, v19, v42
	v_dot2c_f32_bf16_e32 v2, v20, v43
	v_dot2c_f32_bf16_e32 v3, v20, v42
	v_dot2c_f32_bf16_e32 v4, v21, v43
	v_dot2c_f32_bf16_e32 v5, v21, v42
	s_waitcnt vmcnt(1)
	v_dot2c_f32_bf16_e32 v6, v14, v43
	v_dot2c_f32_bf16_e32 v7, v14, v42
	v_dot2c_f32_bf16_e32 v8, v15, v43
	v_dot2c_f32_bf16_e32 v9, v15, v42
	v_dot2c_f32_bf16_e32 v2, v16, v43
	v_dot2c_f32_bf16_e32 v3, v16, v42
	v_dot2c_f32_bf16_e32 v4, v17, v43
	v_dot2c_f32_bf16_e32 v5, v17, v42
	s_waitcnt vmcnt(0)
	v_dot2c_f32_bf16_e32 v6, v10, v43
	v_dot2c_f32_bf16_e32 v7, v10, v42
	v_dot2c_f32_bf16_e32 v8, v11, v43
	v_dot2c_f32_bf16_e32 v9, v11, v42
	v_dot2c_f32_bf16_e32 v2, v12, v43
	v_dot2c_f32_bf16_e32 v3, v12, v42
	v_dot2c_f32_bf16_e32 v4, v13, v43
	v_dot2c_f32_bf16_e32 v5, v13, v42
	s_andn2_b64 exec, exec, s[2:3]
	s_cbranch_execnz .LBB2_354
	s_or_b64 exec, exec, s[2:3]
